# conv1r + quota 3 + MLA K/V LDS-DMA prefetch distance 2 (3-buffer ring)
# speedup vs baseline: 1.0233x; 1.0233x over previous
;     ...
;     int tid = tid_x(); asm volatile("" : "+v"(tid));
;     const int wid = tid >> 6, lane = tid & 63, r32 = lane & 31, hi = lane >> 5;
;     const int qb = uid & 15, h = (uid >> 4) % NH, b = (uid >> 4) / NH;
;     const int tok0 = b * SEQ;
;     const int qrow = tok0 + qb * 256 + wid * 32 + r32;
;     LAS char* V_lds = lds + LDS_VBUF; LAS char* K_lds = lds + LDS_KBUF;
;     LAS float* ws = (LAS float*)(lds + LDS_WS) + wid * 64; LAS float* li_l = ws; LAS float* al_l = ws + 32;
;     LAS float* rpbL = (LAS float*)(lds + LDS_RPB);
;     const int sr = tid >> 4, sc = (tid & 15) * 8, vst0 = v_st(sr, sc), vst1 = v_st(32 + sr, sc);
;     const int sr64 = tid >> 3, sc64 = (tid & 7) * 8;
;     const int vb0 = (int)(unsigned)(uintptr_t)V_lds + v_rd_base(lane);
;     int NT = 64, kbase = tok0;
;     int rq = 0, qc = 0, kr_lo = 0;
;     if constexpr (MODE == MODE_NA) { const int rq0 = qb * 4; kr_lo = min(min(max(rq0 - 4, 0), 56), 52); NT = 12; kbase = tok0 + kr_lo * 64; rq = rq0 + (wid >> 1); qc = (wid & 1) * 32 + r32;
;         for (int i = tid; i < 15 * 31; i += 512) rpbL[i] = P.rpb[h * 465 + i];
;         __syncthreads(); }
;     const bf16* Kg; const bf16* Vg; const bf16* Kg2 = nullptr; int ldk, ldv;
;     if constexpr (MODE == MODE_MLA) { Kg = P.KVM + h * 256; Vg = P.KVM + h * 256 + 128; Kg2 = P.U + U_KR; ldk = KVW; ldv = KVW; }
;     else if constexpr (MODE == MODE_NA) { Kg = P.U + U_NA + 512 + h * 128; Vg = P.U + U_NA + 1024 + h * 128; ldk = UW; ldv = UW; }
;     else { Kg = P.U + U_DF + 512 + h * 128; Vg = P.U + U_DF + 1024 + h * 128; ldk = UW; ldv = UW; }
;     constexpr int pass = PASS;
;     constexpr bool HALF_OFFSET = false;
;     {
;         float m_reg = -1e30f, l_reg = 0; f32x16 o[4] = {}; bf16x8 qr[NQ];
;         if constexpr (MODE == MODE_MLA) {
;             const bf16* Qw = P.QM + (size_t)qrow * QMW + h * 192 + hi * 8;
; #pragma unroll
;             for (int d0 = 0; d0 < 12; ++d0) qr[d0] = *(const bf16x8*)(Qw + d0 * 16);
;             const f32x2* rt = P.ropeM + (size_t)(qrow & (SEQ - 1)) * 32;
; #pragma unroll
;             for (int g = 0; g < 2; ++g) {
;                 bf16x8 x1 = qr[8 + g], x2 = qr[10 + g];
; #pragma unroll
;                 for (int e = 0; e < 8; ++e) { const f32x2 cs = rt[g * 16 + hi * 8 + e];
;                     const float a = bf2f((unsigned short)x1[e]), c = bf2f((unsigned short)x2[e]);
.LBB0_785:
	s_lshl_b32 s0, s22, 1
	s_and_b32 s0, s0, 14
	s_ashr_i32 s1, s22, 7
	s_add_i32 s0, s0, s1
	s_getreg_b32 s1, hwreg(HW_REG_HW_ID, 0, 6)
	s_and_b32 s1, s1, 63
	s_lshl_b32 s1, s1, 2
	s_add_i32 s1, s1, 0
	s_add_i32 s1, s1, 0x23f00
	s_waitcnt vmcnt(15)
	v_mov_b32_e32 v0, s1
	ds_read_b32 v0, v0
	v_mbcnt_lo_u32_b32 v1, -1, 0
	v_mbcnt_hi_u32_b32 v1, -1, v1
	v_mov_b32_e32 v145, v193
	v_mov_b32_e32 v149, v193
	s_movk_i32 s3, 0x70
	s_waitcnt lgkmcnt(0)
	v_readfirstlane_b32 s1, v0
	s_mov_b32 s28, 0
	v_mov_b32_e32 v147, v193
	s_waitcnt vmcnt(13)
	v_lshl_add_u32 v11, s1, 6, v1
	s_lshr_b32 s1, s0, 29
	s_add_i32 s1, s0, s1
	s_and_b32 s2, s1, -8
	s_sub_i32 s23, s0, s2
	s_lshl_b32 s0, s1, 9
	s_and_b32 s4, s0, 0xfffff000
	s_lshl_b32 s0, s22, 5
	s_and_b32 s0, s0, 0xf00
	s_or_b32 s25, s4, s0
	v_ashrrev_i32_e32 v156, 6, v11
	v_and_b32_e32 v154, 31, v11
	v_lshl_add_u32 v0, v156, 5, s25
	v_or_b32_e32 v8, v0, v154
	v_and_b32_e32 v0, 0x3fffffc0, v11
	s_add_i32 s0, 0, 0x1e000
	v_lshl_add_u32 v157, v0, 2, s0
	s_lshl_b32 s0, s23, 8
	s_ashr_i32 s1, s0, 31
	s_lshl_b64 s[0:1], s[0:1], 1
	s_add_u32 s26, s18, s0
	v_mov_b64_e32 v[0:1], s[10:11]
	s_movk_i32 s0, 0xc00
	s_addc_u32 s27, s19, s1
	v_mad_i64_i32 v[0:1], s[0:1], v8, s0, v[0:1]
	s_mul_i32 s0, s23, 0xc0
	v_lshlrev_b32_e32 v8, 8, v8
	v_bfe_u32 v155, v11, 5, 1
	s_ashr_i32 s1, s0, 31
	v_and_b32_e32 v192, 0xfff00, v8
	v_lshl_add_u64 v[0:1], s[0:1], 1, v[0:1]
	v_lshlrev_b32_e32 v144, 4, v155
	v_lshl_add_u64 v[8:9], s[12:13], 0, v[192:193]
	v_lshlrev_b32_e32 v192, 6, v155
	v_lshl_add_u64 v[4:5], v[0:1], 0, v[144:145]
	v_lshl_add_u64 v[8:9], v[8:9], 0, v[192:193]
	global_load_dwordx4 v[96:99], v[4:5], off
	global_load_dwordx4 v[100:103], v[4:5], off offset:32
	global_load_dwordx4 v[104:107], v[4:5], off offset:64
	global_load_dwordx4 v[108:111], v[4:5], off offset:96
	global_load_dwordx4 v[112:115], v[4:5], off offset:128
	global_load_dwordx4 v[116:119], v[4:5], off offset:160
	global_load_dwordx4 v[120:123], v[4:5], off offset:192
	global_load_dwordx4 v[124:127], v[4:5], off offset:224
	global_load_dwordx4 v[26:29], v[4:5], off offset:256
	global_load_dwordx4 v[0:3], v[4:5], off offset:288
	global_load_dwordx4 v[30:33], v[4:5], off offset:320
	s_nop 0
	global_load_dwordx4 v[4:7], v[4:5], off offset:352
	s_waitcnt vmcnt(24)
	v_lshlrev_b32_e32 v13, 4, v11
	global_load_dwordx2 v[14:15], v[8:9], off
	v_readfirstlane_b32 s0, v156
	s_ashr_i32 s5, s4, 31
	s_lshl_b32 s2, s0, 10
	s_lshl_b64 s[0:1], s[4:5], 12
	s_add_u32 s0, s26, s0
	s_addc_u32 s1, s27, s1
	s_add_i32 s29, s2, 0
	s_mov_b32 m0, s29
	s_add_i32 s2, s29, 0xc000
	v_and_b32_e32 v10, 63, v11
	v_and_b32_e32 v12, 0xc0, v13
	v_mov_b32_e32 v151, v193
	v_lshlrev_b32_e32 v145, 8, v154
	v_lshlrev_b32_e32 v167, 7, v154
	v_lshl_add_u32 v163, v154, 2, v157
	v_mov_b32_e32 v174, 0
	v_mov_b32_e32 v173, 0xf149f2ca
	s_waitcnt vmcnt(4)
	v_lshlrev_b32_e32 v17, 16, v26
	s_waitcnt vmcnt(2)
	v_lshlrev_b32_e32 v16, 16, v30
	s_waitcnt vmcnt(0)
	v_pk_mul_f32 v[18:19], v[14:15], v[16:17] op_sel:[0,1] op_sel_hi:[1,0]
	v_pk_mul_f32 v[14:15], v[14:15], v[16:17]
	v_sub_f32_e32 v18, v18, v19
	v_add_f32_e32 v14, v15, v14
	v_cvt_pk_bf16_f32 v15, v18, v193
	v_cvt_pk_bf16_f32 v14, v14, v193
	global_load_dwordx2 v[16:17], v[8:9], off offset:8
	v_and_b32_e32 v19, 0xffff0000, v26
	v_and_b32_e32 v18, 0xffff0000, v30
	s_waitcnt vmcnt(0)
	v_pk_mul_f32 v[20:21], v[16:17], v[18:19] op_sel:[0,1] op_sel_hi:[1,0]
	v_pk_mul_f32 v[16:17], v[16:17], v[18:19]
	v_sub_f32_e32 v20, v20, v21
	v_add_f32_e32 v16, v16, v17
	v_cvt_pk_bf16_f32 v17, v20, v193
	v_cvt_pk_bf16_f32 v16, v16, v193
	global_load_dwordx2 v[18:19], v[8:9], off offset:16
	v_lshlrev_b32_e32 v21, 16, v27
	v_lshlrev_b32_e32 v20, 16, v31
	s_waitcnt vmcnt(0)
	v_pk_mul_f32 v[22:23], v[18:19], v[20:21] op_sel:[0,1] op_sel_hi:[1,0]
	v_pk_mul_f32 v[18:19], v[18:19], v[20:21]
	v_sub_f32_e32 v22, v22, v23
	v_add_f32_e32 v18, v18, v19
	v_cvt_pk_bf16_f32 v19, v22, v193
	v_cvt_pk_bf16_f32 v18, v18, v193
	global_load_dwordx2 v[20:21], v[8:9], off offset:24
	v_and_b32_e32 v23, 0xffff0000, v27
	v_and_b32_e32 v22, 0xffff0000, v31
	s_waitcnt vmcnt(0)
	v_pk_mul_f32 v[24:25], v[20:21], v[22:23] op_sel:[0,1] op_sel_hi:[1,0]
	v_pk_mul_f32 v[20:21], v[20:21], v[22:23]
	v_sub_f32_e32 v24, v24, v25
	v_add_f32_e32 v20, v20, v21
	v_cvt_pk_bf16_f32 v21, v24, v193
	v_cvt_pk_bf16_f32 v20, v20, v193
	global_load_dwordx2 v[22:23], v[8:9], off offset:32
	v_lshlrev_b32_e32 v25, 16, v28
	v_lshlrev_b32_e32 v24, 16, v32
	s_waitcnt vmcnt(0)
	v_pk_mul_f32 v[26:27], v[22:23], v[24:25] op_sel:[0,1] op_sel_hi:[1,0]
	v_pk_mul_f32 v[22:23], v[22:23], v[24:25]
	v_sub_f32_e32 v26, v26, v27
	v_add_f32_e32 v22, v22, v23
	v_cvt_pk_bf16_f32 v23, v26, v193
	v_cvt_pk_bf16_f32 v22, v22, v193
	global_load_dwordx2 v[24:25], v[8:9], off offset:40
	v_and_b32_e32 v27, 0xffff0000, v28
	v_and_b32_e32 v26, 0xffff0000, v32
	s_waitcnt vmcnt(0)
	v_pk_mul_f32 v[30:31], v[24:25], v[26:27] op_sel:[0,1] op_sel_hi:[1,0]
	v_pk_mul_f32 v[24:25], v[24:25], v[26:27]
	v_sub_f32_e32 v28, v30, v31
	v_add_f32_e32 v24, v24, v25
	v_cvt_pk_bf16_f32 v25, v28, v193
	v_cvt_pk_bf16_f32 v24, v24, v193
	global_load_dwordx2 v[26:27], v[8:9], off offset:48
	v_lshlrev_b32_e32 v31, 16, v29
	v_lshlrev_b32_e32 v30, 16, v33
	v_and_b32_e32 v29, 0xffff0000, v29
	s_waitcnt vmcnt(0)
	v_pk_mul_f32 v[34:35], v[26:27], v[30:31] op_sel:[0,1] op_sel_hi:[1,0]
	v_pk_mul_f32 v[26:27], v[26:27], v[30:31]
	v_sub_f32_e32 v28, v34, v35
	v_add_f32_e32 v26, v26, v27
	v_cvt_pk_bf16_f32 v27, v28, v193
	v_cvt_pk_bf16_f32 v26, v26, v193
	global_load_dwordx2 v[30:31], v[8:9], off offset:56
	v_and_b32_e32 v28, 0xffff0000, v33
	v_lshlrev_b32_e32 v35, 16, v0
	v_lshlrev_b32_e32 v34, 16, v4
	s_waitcnt vmcnt(0)
; __device__ __forceinline__ unsigned cvt_pk_bf16(float lo, float hi) { unsigned r; asm volatile("v_cvt_pk_bf16_f32 %0, %1, %2" : "=v"(r) : "v"(lo), "v"(hi)); return r; }
;     ...
;             const f32x2* rt = P.ropeM + (size_t)(qrow & (SEQ - 1)) * 32;
; #pragma unroll
;             for (int g = 0; g < 2; ++g) {
;                 bf16x8 x1 = qr[8 + g], x2 = qr[10 + g];
; #pragma unroll
;                 for (int e = 0; e < 8; ++e) { const f32x2 cs = rt[g * 16 + hi * 8 + e];
;                     const float a = bf2f((unsigned short)x1[e]), c = bf2f((unsigned short)x2[e]);
;                     const float ra = a * cs.x - c * cs.y, rc = c * cs.x + a * cs.y;
;                     x1[e] = (short)(cvt_pk_bf16(ra, 0.f) & 0xffffu); x2[e] = (short)(cvt_pk_bf16(rc, 0.f) & 0xffffu); }
;                 qr[8 + g] = x1; qr[10 + g] = x2;
;             }
	v_pk_mul_f32 v[32:33], v[30:31], v[28:29] op_sel:[0,1] op_sel_hi:[1,0]
	v_pk_mul_f32 v[28:29], v[30:31], v[28:29]
	v_sub_f32_e32 v32, v32, v33
	v_add_f32_e32 v28, v28, v29
	v_cvt_pk_bf16_f32 v30, v32, v193
	v_cvt_pk_bf16_f32 v28, v28, v193
	global_load_dwordx2 v[32:33], v[8:9], off offset:128
	s_waitcnt vmcnt(0)
	v_pk_mul_f32 v[36:37], v[32:33], v[34:35] op_sel:[0,1] op_sel_hi:[1,0]
	v_pk_mul_f32 v[32:33], v[32:33], v[34:35]
	v_sub_f32_e32 v29, v36, v37
	v_add_f32_e32 v32, v32, v33
	v_cvt_pk_bf16_f32 v31, v29, v193
	v_cvt_pk_bf16_f32 v29, v32, v193
	global_load_dwordx2 v[32:33], v[8:9], off offset:136
	v_and_b32_e32 v35, 0xffff0000, v0
	v_and_b32_e32 v34, 0xffff0000, v4
	s_waitcnt vmcnt(0)
	v_pk_mul_f32 v[36:37], v[32:33], v[34:35] op_sel:[0,1] op_sel_hi:[1,0]
	v_pk_mul_f32 v[32:33], v[32:33], v[34:35]
	v_sub_f32_e32 v0, v36, v37
	v_add_f32_e32 v4, v32, v33
	v_cvt_pk_bf16_f32 v32, v0, v193
	v_cvt_pk_bf16_f32 v4, v4, v193
	global_load_dwordx2 v[34:35], v[8:9], off offset:144
	v_lshlrev_b32_e32 v37, 16, v1
	v_lshlrev_b32_e32 v36, 16, v5
	v_and_b32_e32 v1, 0xffff0000, v1
	s_waitcnt vmcnt(0)
	v_pk_mul_f32 v[38:39], v[34:35], v[36:37] op_sel:[0,1] op_sel_hi:[1,0]
	v_pk_mul_f32 v[34:35], v[34:35], v[36:37]
	v_sub_f32_e32 v0, v38, v39
	v_add_f32_e32 v33, v34, v35
	v_cvt_pk_bf16_f32 v34, v0, v193
	v_cvt_pk_bf16_f32 v33, v33, v193
	global_load_dwordx2 v[36:37], v[8:9], off offset:152
	v_and_b32_e32 v0, 0xffff0000, v5
	s_waitcnt vmcnt(0)
	v_pk_mul_f32 v[38:39], v[36:37], v[0:1] op_sel:[0,1] op_sel_hi:[1,0]
	v_pk_mul_f32 v[0:1], v[36:37], v[0:1]
	v_sub_f32_e32 v5, v38, v39
	v_add_f32_e32 v0, v0, v1
	v_cvt_pk_bf16_f32 v35, v5, v193
	v_cvt_pk_bf16_f32 v5, v0, v193
	global_load_dwordx2 v[0:1], v[8:9], off offset:160
	v_lshlrev_b32_e32 v37, 16, v2
	v_lshlrev_b32_e32 v36, 16, v6
	s_waitcnt vmcnt(0)
	v_pk_mul_f32 v[38:39], v[0:1], v[36:37] op_sel:[0,1] op_sel_hi:[1,0]
	v_pk_mul_f32 v[0:1], v[0:1], v[36:37]
	v_sub_f32_e32 v38, v38, v39
	v_add_f32_e32 v0, v0, v1
	v_cvt_pk_bf16_f32 v37, v38, v193
	v_cvt_pk_bf16_f32 v36, v0, v193
	global_load_dwordx2 v[0:1], v[8:9], off offset:168
	v_and_b32_e32 v39, 0xffff0000, v2
	v_and_b32_e32 v38, 0xffff0000, v6
	s_waitcnt vmcnt(0)
	v_pk_mul_f32 v[40:41], v[0:1], v[38:39] op_sel:[0,1] op_sel_hi:[1,0]
	v_pk_mul_f32 v[0:1], v[0:1], v[38:39]
	v_sub_f32_e32 v2, v40, v41
	v_add_f32_e32 v0, v0, v1
	v_cvt_pk_bf16_f32 v6, v2, v193
	v_cvt_pk_bf16_f32 v2, v0, v193
	global_load_dwordx2 v[0:1], v[8:9], off offset:176
	v_lshlrev_b32_e32 v39, 16, v3
	v_lshlrev_b32_e32 v38, 16, v7
	s_waitcnt vmcnt(0)
	v_pk_mul_f32 v[40:41], v[0:1], v[38:39] op_sel:[0,1] op_sel_hi:[1,0]
	v_pk_mul_f32 v[0:1], v[0:1], v[38:39]
	v_sub_f32_e32 v40, v40, v41
	v_add_f32_e32 v0, v0, v1
	v_cvt_pk_bf16_f32 v39, v40, v193
	v_cvt_pk_bf16_f32 v38, v0, v193
	global_load_dwordx2 v[0:1], v[8:9], off offset:184
	v_and_b32_e32 v9, 0xffff0000, v3
	v_and_b32_e32 v8, 0xffff0000, v7
	s_waitcnt vmcnt(0)
; #define VM_WAIT() asm volatile("s_waitcnt vmcnt(0)" ::: "memory")
; #define SBAR() __builtin_amdgcn_sched_barrier(0)
;     ...
;         } else if constexpr (ATT_GLDS) {
;         unsigned gsv[2], gsk[2], gsk2 = 0u;
; #pragma unroll
;         for (int i = 0; i < 2; ++i) { const int a = (i * 512 + tid) * 16;
;             { const int sub = a >> 9, within = a & 511; const int kk = (sub >> 2) * 8 + (within >> 6); const int k = (kk & ~0xC) | ((kk & 4) << 1) | ((kk & 8) >> 1);
;               const int c = (sub & 3) * 32 + ((within & 63) >> 1); gsv[i] = (unsigned)(k * ldv + c) * 2u; }
;             if constexpr (MODE == MODE_DIFF) { if (i == 0) { const int row = a >> 7, ch = ((a >> 4) & 7) ^ ((row >> 1) & 7); gsk[0] = (unsigned)(row * ldk + ch * 8) * 2u; } gsk[1] = 0u; }
;             else { const int row = a >> 8, ch = ((a >> 4) & 15) ^ (row & 15); gsk[i] = (unsigned)(row * ldk + ch * 8) * 2u; } }
;         if constexpr (MODE == MODE_MLA) { const int a = tid * 16, row = a >> 7, ch = ((a >> 4) & 7) ^ ((row >> 1) & 7); gsk2 = (unsigned)(row * UW + ch * 8) * 2u; }
;         const unsigned ldsw = (unsigned)__builtin_amdgcn_readfirstlane(wid) * 1024u;
;     ...
;         GLDS(0, 0); VM_WAIT(); __syncthreads();
; #pragma unroll 1
;         for (int t = 0; t < NT; ++t) {
;             const int bf = t & 1;
;             if (t + 1 < NT) GLDS(t + 1, bf ^ 1);
;             SBAR();
	v_pk_mul_f32 v[40:41], v[0:1], v[8:9] op_sel:[0,1] op_sel_hi:[1,0]
	v_pk_mul_f32 v[0:1], v[0:1], v[8:9]
	v_sub_f32_e32 v3, v40, v41
	v_add_f32_e32 v0, v0, v1
	v_bfe_i32 v9, v11, 4, 24
	v_cvt_pk_bf16_f32 v8, v3, v193
	v_cvt_pk_bf16_f32 v7, v0, v193
	v_bfe_u32 v0, v11, 2, 2
	v_lshrrev_b32_e32 v1, 1, v11
	v_lshlrev_b32_e32 v3, 1, v11
	v_lshrrev_b32_e32 v41, 1, v9
	v_and_or_b32 v0, v1, 8, v0
	v_and_b32_e32 v1, 0xc0, v3
	v_and_b32_e32 v40, 0xffff0, v9
	v_and_b32_e32 v41, 4, v41
	v_and_or_b32 v1, v13, 48, v1
	v_or3_b32 v40, v40, v41, v0
	v_lshl_or_b32 v192, v40, 12, v1
	v_xor_b32_e32 v40, v9, v11
	v_lshlrev_b32_e32 v9, 12, v9
	v_lshlrev_b32_e32 v40, 4, v40
	v_and_or_b32 v146, v40, s87, v9
	v_add_u32_e32 v9, 0x2000, v13
	v_ashrrev_i32_e32 v9, 8, v9
	v_lshrrev_b32_e32 v41, 1, v9
	v_and_b32_e32 v40, 0xffff0, v9
	v_and_b32_e32 v41, 4, v41
	v_or3_b32 v0, v40, v41, v0
	v_lshl_add_u64 v[40:41], s[0:1], 0, v[192:193]
	v_lshl_or_b32 v148, v0, 12, v1
	v_lshl_add_u64 v[40:41], v[40:41], 0, s[36:37]
	global_load_lds_dwordx4 v[40:41], off
	v_lshl_add_u64 v[40:41], s[0:1], 0, v[148:149]
	v_xor_b32_e32 v0, v9, v11
	v_lshl_add_u64 v[40:41], v[40:41], 0, s[36:37]
	s_add_i32 m0, s29, 0x2000
	v_lshlrev_b32_e32 v1, 12, v9
	v_lshlrev_b32_e32 v0, 4, v0
	global_load_lds_dwordx4 v[40:41], off
	s_mov_b32 m0, s2
	v_and_or_b32 v150, v0, s87, v1
	global_load_lds_dwordx4 v146, s[0:1]
	s_add_i32 m0, s29, 0xe000
	v_lshlrev_b32_e32 v0, 10, v11
	global_load_lds_dwordx4 v150, s[0:1]
	s_lshl_b64 s[0:1], s[4:5], 13
	v_and_b32_e32 v0, 0xffffe000, v0
	v_xor_b32_e32 v1, v13, v11
	s_add_u32 s0, s14, s0
	v_and_or_b32 v0, v1, s3, v0
	s_addc_u32 s1, s15, s1
	s_add_i32 m0, s29, 0x10000
	v_mov_b32_e32 v1, v193
	global_load_lds_dwordx4 v0, s[0:1]
	v_lshl_add_u64 v[152:153], s[14:15], 0, v[0:1]
	v_bitop3_b32 v0, v155, v11, 15 bitop3:0x78
	v_lshlrev_b32_e32 v9, 3, v11
	v_lshlrev_b32_e32 v158, 4, v0
	v_and_b32_e32 v0, 0xf0, v13
	v_bitop3_b32 v159, v144, v0, 32 bitop3:0x36
	v_bitop3_b32 v160, v144, v0, 64 bitop3:0x36
	v_bitop3_b32 v161, v144, v0, s60 bitop3:0x36
	v_bitop3_b32 v162, v144, v0, s59 bitop3:0x36
	v_bitop3_b32 v164, v144, v0, s61 bitop3:0x36
	v_bitop3_b32 v165, v144, v0, s58 bitop3:0x36
	v_bitop3_b32 v166, v144, v0, s62 bitop3:0x36
	v_and_b32_e32 v0, 0x70, v9
	v_bitop3_b32 v169, v144, v0, 32 bitop3:0x36
	v_bitop3_b32 v170, v144, v0, 64 bitop3:0x36
	v_bitop3_b32 v171, v144, v0, s60 bitop3:0x36
	v_and_b32_e32 v0, 0x118, v9
	s_mov_b32 s0, 0x5040100
	s_waitcnt vmcnt(0)
	v_perm_b32 v128, v17, v15, s0
	v_perm_b32 v136, v16, v14, s0
	v_and_or_b32 v0, v3, 32, v0
	v_mov_b32_e32 v14, v193
	v_mov_b32_e32 v15, v193
	v_bitop3_b32 v168, v144, v9, s3 bitop3:0x78
	v_cmp_gt_u32_e64 s[2:3], 32, v10
	v_perm_b32 v129, v21, v19, s0
	v_perm_b32 v130, v25, v23, s0
	v_perm_b32 v131, v30, v27, s0
	v_perm_b32 v132, v32, v31, s0
	v_perm_b32 v133, v35, v34, s0
	v_perm_b32 v134, v6, v37, s0
	v_perm_b32 v135, v8, v39, s0
	v_perm_b32 v137, v20, v18, s0
	v_perm_b32 v138, v24, v22, s0
	v_perm_b32 v139, v28, v26, s0
	v_perm_b32 v140, v4, v29, s0
	v_perm_b32 v141, v5, v33, s0
	v_perm_b32 v142, v2, v36, s0
	v_perm_b32 v143, v7, v38, s0
	v_add3_u32 v172, v12, 0, v0
	v_mov_b32_e32 v0, v193
	v_mov_b32_e32 v2, v193
	v_mov_b32_e32 v3, v193
	v_mov_b32_e32 v4, v193
	v_mov_b32_e32 v5, v193
	v_mov_b32_e32 v6, v193
	v_mov_b32_e32 v7, v193
	v_mov_b32_e32 v8, v193
	v_mov_b32_e32 v9, v193
	v_mov_b32_e32 v10, v193
	v_mov_b32_e32 v11, v193
	v_mov_b32_e32 v12, v193
	v_mov_b32_e32 v13, v193
	v_mov_b64_e32 v[30:31], v[14:15]
	v_mov_b64_e32 v[46:47], v[14:15]
	v_mov_b64_e32 v[62:63], v[14:15]
	s_or_b32 s16, s4, 64
	v_mov_b64_e32 v[28:29], v[12:13]
	v_mov_b64_e32 v[26:27], v[10:11]
	v_mov_b64_e32 v[24:25], v[8:9]
	v_mov_b64_e32 v[22:23], v[6:7]
	v_mov_b64_e32 v[20:21], v[4:5]
	v_mov_b64_e32 v[18:19], v[2:3]
	v_mov_b64_e32 v[16:17], v[0:1]
	v_mov_b64_e32 v[44:45], v[12:13]
	v_mov_b64_e32 v[42:43], v[10:11]
	v_mov_b64_e32 v[40:41], v[8:9]
	v_mov_b64_e32 v[38:39], v[6:7]
	v_mov_b64_e32 v[36:37], v[4:5]
	v_mov_b64_e32 v[34:35], v[2:3]
	v_mov_b64_e32 v[32:33], v[0:1]
	v_mov_b64_e32 v[60:61], v[12:13]
	v_mov_b64_e32 v[58:59], v[10:11]
	v_mov_b64_e32 v[56:57], v[8:9]
	v_mov_b64_e32 v[54:55], v[6:7]
	v_mov_b64_e32 v[52:53], v[4:5]
	v_mov_b64_e32 v[50:51], v[2:3]
	v_mov_b64_e32 v[48:49], v[0:1]
	s_waitcnt vmcnt(0) lgkmcnt(0)
	s_barrier
	s_mov_b32 s30, 0
	s_branch .LBB0_787

; #define VM_WAIT() asm volatile("s_waitcnt vmcnt(0)" ::: "memory")
;     ...
;         GLDS(0, 0); VM_WAIT(); __syncthreads();
; #pragma unroll 1
;         for (int t = 0; t < NT; ++t) {
;             const int bf = t & 1;
;             if (t + 1 < NT) GLDS(t + 1, bf ^ 1);
.LBB0_787:
	s_cmp_gt_u32 s28, 61
	s_cbranch_scc1 .LBB0_788
	s_cmp_eq_u32 s28, 0
	s_cselect_b32 s100, 1, 0
	s_add_i32 s4, s30, 2
	s_cmp_ge_u32 s4, 3
	s_cselect_b32 s101, 3, 0
	s_sub_u32 s4, s4, s101
	s_cmp_eq_u32 s100, 1
	s_cselect_b32 s4, 1, s4
.Lpf_more:
	s_ashr_i32 s17, s16, 31
	s_lshl_b64 s[0:1], s[16:17], 12
	s_add_u32 s0, s26, s0
	s_addc_u32 s1, s27, s1
	s_lshl_b32 s5, s4, 14
	s_add_i32 s5, s29, s5
	v_lshl_add_u64 v[64:65], s[0:1], 0, v[192:193]
	s_mulk_i32 s4, 0x6000
	v_lshl_add_u64 v[64:65], v[64:65], 0, s[36:37]
	s_mov_b32 m0, s5
	s_add_i32 s4, s29, s4
	global_load_lds_dwordx4 v[64:65], off
	v_lshl_add_u64 v[64:65], s[0:1], 0, v[148:149]
	s_add_i32 s31, s4, 0xc000
	v_lshl_add_u64 v[64:65], v[64:65], 0, s[36:37]
	s_add_i32 m0, s5, 0x2000
	s_nop 0
	global_load_lds_dwordx4 v[64:65], off
	v_lshl_add_u64 v[64:65], s[0:1], 0, v[146:147]
	s_mov_b32 m0, s31
	s_nop 0
	global_load_lds_dwordx4 v[64:65], off
	v_lshl_add_u64 v[64:65], s[0:1], 0, v[150:151]
	s_add_i32 m0, s4, 0xe000
	s_lshl_b64 s[0:1], s[16:17], 13
	global_load_lds_dwordx4 v[64:65], off
	v_lshl_add_u64 v[64:65], v[152:153], 0, s[0:1]
	s_add_i32 m0, s4, 0x10000
	s_nop 0
	global_load_lds_dwordx4 v[64:65], off
	s_add_i32 s16, s16, 64
	s_cmp_eq_u32 s100, 1
	s_cbranch_scc0 .LBB0_788
	s_mov_b32 s100, 0
	s_mov_b32 s4, 2
	s_branch .Lpf_more
